# P1 pool-GEMM epilogue: f32 residual loads issued 8 groups ahead into a register ring, counted vmcnt; s_nop after x4 stores
# speedup vs baseline: 1.0187x; 1.0089x over previous
.LBB0_352:
	s_mov_b64 s[98:99], 0x20000
	s_lshl_b32 s2, s36, 8
	s_add_i32 s2, s2, s49
	v_and_or_b32 v164, v164, 15, s2
	v_ashrrev_i32_e32 v165, 31, v164
	v_lshlrev_b64 v[160:161], 11, v[164:165]
	v_lshl_add_u64 v[160:161], v[160:161], 0, v[162:163]
	v_lshl_add_u64 v[178:179], v[160:161], 2, s[6:7]
	global_load_dwordx4 v[170:173], v[178:179], off
	global_load_dwordx4 v[174:177], v[178:179], off offset:16
	global_load_dwordx4 v[182:185], v[178:179], off offset:512
	global_load_dwordx4 v[186:189], v[178:179], off offset:528
	v_lshl_add_u64 v[246:247], v[178:179], 0, s[98:99]
	global_load_dwordx4 v[190:193], v[246:247], off
	global_load_dwordx4 v[194:197], v[246:247], off offset:16
	v_lshl_add_u64 v[246:247], v[178:179], 0, s[98:99]
	global_load_dwordx4 v[198:201], v[246:247], off offset:512
	global_load_dwordx4 v[202:205], v[246:247], off offset:528
	v_lshl_add_u64 v[246:247], v[178:179], 0, s[98:99]
	v_lshl_add_u64 v[246:247], v[246:247], 0, s[98:99]
	global_load_dwordx4 v[206:209], v[246:247], off
	global_load_dwordx4 v[210:213], v[246:247], off offset:16
	v_lshl_add_u64 v[246:247], v[178:179], 0, s[98:99]
	v_lshl_add_u64 v[246:247], v[246:247], 0, s[98:99]
	global_load_dwordx4 v[214:217], v[246:247], off offset:512
	global_load_dwordx4 v[218:221], v[246:247], off offset:528
	v_lshl_add_u64 v[246:247], v[178:179], 0, s[98:99]
	v_lshl_add_u64 v[246:247], v[246:247], 0, s[98:99]
	v_lshl_add_u64 v[246:247], v[246:247], 0, s[98:99]
	global_load_dwordx4 v[222:225], v[246:247], off
	global_load_dwordx4 v[226:229], v[246:247], off offset:16
	v_lshl_add_u64 v[246:247], v[178:179], 0, s[98:99]
	v_lshl_add_u64 v[246:247], v[246:247], 0, s[98:99]
	v_lshl_add_u64 v[246:247], v[246:247], 0, s[98:99]
	global_load_dwordx4 v[230:233], v[246:247], off offset:512
	global_load_dwordx4 v[234:237], v[246:247], off offset:528
	v_lshl_add_u64 v[246:247], v[160:161], 0, s[20:21]
	v_lshl_add_u64 v[246:247], v[246:247], 2, s[6:7]
	global_load_dwordx4 v[238:241], v[246:247], off
	global_load_dwordx4 v[242:245], v[246:247], off offset:16
	v_lshl_add_u64 v[180:181], v[160:161], 1, s[64:65]
	s_andn2_b64 vcc, exec, s[0:1]
	s_mov_b64 s[0:1], -1
	s_waitcnt vmcnt(16)
	v_pk_mul_f32 v[170:171], v[170:171], s[18:19] op_sel_hi:[1,0]
	v_pk_mul_f32 v[176:177], v[176:177], s[18:19] op_sel_hi:[1,0]
	v_pk_mul_f32 v[174:175], v[174:175], s[18:19] op_sel_hi:[1,0]
	v_pk_mul_f32 v[172:173], v[172:173], s[18:19] op_sel_hi:[1,0]
	v_pk_fma_f32 v[140:141], v[140:141], v[132:133], v[170:171]
	v_pk_fma_f32 v[170:171], v[138:139], v[130:131], v[176:177]
	v_pk_fma_f32 v[138:139], v[136:137], v[128:129], v[174:175]
	v_pk_fma_f32 v[142:143], v[142:143], v[134:135], v[172:173]
	v_cvt_pk_bf16_f32 v136, v140, v141
	s_nop 0
	v_cvt_pk_bf16_f32 v137, v142, v143
	v_cvt_pk_bf16_f32 v138, v138, v139
	v_cvt_pk_bf16_f32 v139, v170, v171
	global_store_dwordx4 v[180:181], v[136:139], off
	s_nop 1
	v_or_b32_e32 v170, 16, v164
	v_ashrrev_i32_e32 v171, 31, v170
	v_lshlrev_b64 v[170:171], 11, v[170:171]
	v_lshl_add_u64 v[170:171], v[170:171], 0, v[162:163]
	s_waitcnt vmcnt(16)
	v_pk_mul_f32 v[136:137], v[182:183], s[18:19] op_sel_hi:[1,0]
	s_waitcnt vmcnt(15)
	v_pk_mul_f32 v[142:143], v[188:189], s[18:19] op_sel_hi:[1,0]
	v_pk_mul_f32 v[140:141], v[186:187], s[18:19] op_sel_hi:[1,0]
	v_pk_mul_f32 v[138:139], v[184:185], s[18:19] op_sel_hi:[1,0]
	v_lshl_add_u64 v[246:247], v[160:161], 0, s[20:21]
	v_lshl_add_u64 v[246:247], v[246:247], 2, s[6:7]
	global_load_dwordx4 v[182:185], v[246:247], off offset:512
	global_load_dwordx4 v[186:189], v[246:247], off offset:528
	v_pk_fma_f32 v[116:117], v[116:117], v[124:125], v[136:137]
	v_pk_fma_f32 v[136:137], v[114:115], v[122:123], v[142:143]
	v_pk_fma_f32 v[114:115], v[112:113], v[120:121], v[140:141]
	v_pk_fma_f32 v[118:119], v[118:119], v[126:127], v[138:139]
	v_cvt_pk_bf16_f32 v112, v116, v117
	s_nop 0
	v_cvt_pk_bf16_f32 v113, v118, v119
	v_cvt_pk_bf16_f32 v114, v114, v115
	v_cvt_pk_bf16_f32 v115, v136, v137
	global_store_dwordx4 v[180:181], v[112:115], off offset:256
	s_nop 1
	v_lshl_add_u64 v[136:137], v[170:171], 1, s[64:65]
	s_waitcnt vmcnt(17)
	v_pk_mul_f32 v[112:113], v[190:191], s[18:19] op_sel_hi:[1,0]
	s_waitcnt vmcnt(16)
	v_pk_mul_f32 v[118:119], v[196:197], s[18:19] op_sel_hi:[1,0]
	v_pk_mul_f32 v[116:117], v[194:195], s[18:19] op_sel_hi:[1,0]
	v_pk_mul_f32 v[114:115], v[192:193], s[18:19] op_sel_hi:[1,0]
	v_lshl_add_u64 v[246:247], v[160:161], 0, s[22:23]
	v_lshl_add_u64 v[246:247], v[246:247], 2, s[6:7]
	global_load_dwordx4 v[190:193], v[246:247], off
	global_load_dwordx4 v[194:197], v[246:247], off offset:16
	v_pk_fma_f32 v[108:109], v[108:109], v[132:133], v[112:113]
	v_pk_fma_f32 v[112:113], v[106:107], v[130:131], v[118:119]
	v_pk_fma_f32 v[106:107], v[104:105], v[128:129], v[116:117]
	v_pk_fma_f32 v[110:111], v[110:111], v[134:135], v[114:115]
	v_cvt_pk_bf16_f32 v104, v108, v109
	s_nop 0
	v_cvt_pk_bf16_f32 v105, v110, v111
	v_cvt_pk_bf16_f32 v106, v106, v107
	v_cvt_pk_bf16_f32 v107, v112, v113
	global_store_dwordx4 v[136:137], v[104:107], off
	s_nop 1
	v_or_b32_e32 v112, 32, v164
	v_ashrrev_i32_e32 v113, 31, v112
	v_lshlrev_b64 v[112:113], 11, v[112:113]
	v_lshl_add_u64 v[112:113], v[112:113], 0, v[162:163]
	s_waitcnt vmcnt(18)
	v_pk_mul_f32 v[104:105], v[198:199], s[18:19] op_sel_hi:[1,0]
	s_waitcnt vmcnt(17)
	v_pk_mul_f32 v[110:111], v[204:205], s[18:19] op_sel_hi:[1,0]
	v_pk_mul_f32 v[108:109], v[202:203], s[18:19] op_sel_hi:[1,0]
	v_pk_mul_f32 v[106:107], v[200:201], s[18:19] op_sel_hi:[1,0]
	v_lshl_add_u64 v[246:247], v[160:161], 0, s[22:23]
	v_lshl_add_u64 v[246:247], v[246:247], 2, s[6:7]
	global_load_dwordx4 v[198:201], v[246:247], off offset:512
	global_load_dwordx4 v[202:205], v[246:247], off offset:528
	v_pk_fma_f32 v[100:101], v[100:101], v[124:125], v[104:105]
	v_pk_fma_f32 v[104:105], v[98:99], v[122:123], v[110:111]
	v_pk_fma_f32 v[98:99], v[96:97], v[120:121], v[108:109]
	v_pk_fma_f32 v[102:103], v[102:103], v[126:127], v[106:107]
	v_cvt_pk_bf16_f32 v96, v100, v101
	s_nop 0
	v_cvt_pk_bf16_f32 v97, v102, v103
	v_cvt_pk_bf16_f32 v98, v98, v99
	v_cvt_pk_bf16_f32 v99, v104, v105
	global_store_dwordx4 v[136:137], v[96:99], off offset:256
	s_nop 1
	v_lshl_add_u64 v[104:105], v[112:113], 1, s[64:65]
	s_waitcnt vmcnt(19)
	v_pk_mul_f32 v[96:97], v[206:207], s[18:19] op_sel_hi:[1,0]
	s_waitcnt vmcnt(18)
	v_pk_mul_f32 v[102:103], v[212:213], s[18:19] op_sel_hi:[1,0]
	v_pk_mul_f32 v[100:101], v[210:211], s[18:19] op_sel_hi:[1,0]
	v_pk_mul_f32 v[98:99], v[208:209], s[18:19] op_sel_hi:[1,0]
	v_lshl_add_u64 v[246:247], v[160:161], 0, s[24:25]
	v_lshl_add_u64 v[246:247], v[246:247], 2, s[6:7]
	global_load_dwordx4 v[206:209], v[246:247], off
	global_load_dwordx4 v[210:213], v[246:247], off offset:16
	v_pk_fma_f32 v[92:93], v[92:93], v[132:133], v[96:97]
	v_pk_fma_f32 v[96:97], v[90:91], v[130:131], v[102:103]
	v_pk_fma_f32 v[90:91], v[88:89], v[128:129], v[100:101]
	v_pk_fma_f32 v[94:95], v[94:95], v[134:135], v[98:99]
	v_cvt_pk_bf16_f32 v88, v92, v93
	s_nop 0
	v_cvt_pk_bf16_f32 v89, v94, v95
	v_cvt_pk_bf16_f32 v90, v90, v91
	v_cvt_pk_bf16_f32 v91, v96, v97
	global_store_dwordx4 v[104:105], v[88:91], off
	s_nop 1
	v_or_b32_e32 v96, 48, v164
	v_ashrrev_i32_e32 v97, 31, v96
	v_lshlrev_b64 v[96:97], 11, v[96:97]
	v_lshl_add_u64 v[96:97], v[96:97], 0, v[162:163]
	s_waitcnt vmcnt(20)
	v_pk_mul_f32 v[88:89], v[214:215], s[18:19] op_sel_hi:[1,0]
	s_waitcnt vmcnt(19)
	v_pk_mul_f32 v[94:95], v[220:221], s[18:19] op_sel_hi:[1,0]
	v_pk_mul_f32 v[92:93], v[218:219], s[18:19] op_sel_hi:[1,0]
	v_pk_mul_f32 v[90:91], v[216:217], s[18:19] op_sel_hi:[1,0]
	v_lshl_add_u64 v[246:247], v[160:161], 0, s[24:25]
	v_lshl_add_u64 v[246:247], v[246:247], 2, s[6:7]
	global_load_dwordx4 v[214:217], v[246:247], off offset:512
	global_load_dwordx4 v[218:221], v[246:247], off offset:528
	v_pk_fma_f32 v[84:85], v[84:85], v[124:125], v[88:89]
	v_pk_fma_f32 v[88:89], v[82:83], v[122:123], v[94:95]
	v_pk_fma_f32 v[82:83], v[80:81], v[120:121], v[92:93]
	v_pk_fma_f32 v[86:87], v[86:87], v[126:127], v[90:91]
	v_cvt_pk_bf16_f32 v80, v84, v85
	s_nop 0
	v_cvt_pk_bf16_f32 v81, v86, v87
	v_cvt_pk_bf16_f32 v82, v82, v83
	v_cvt_pk_bf16_f32 v83, v88, v89
	global_store_dwordx4 v[104:105], v[80:83], off offset:256
	s_nop 1
	v_lshl_add_u64 v[88:89], v[96:97], 1, s[64:65]
	s_waitcnt vmcnt(21)
	v_pk_mul_f32 v[80:81], v[222:223], s[18:19] op_sel_hi:[1,0]
	s_waitcnt vmcnt(20)
	v_pk_mul_f32 v[86:87], v[228:229], s[18:19] op_sel_hi:[1,0]
	v_pk_mul_f32 v[84:85], v[226:227], s[18:19] op_sel_hi:[1,0]
	v_pk_mul_f32 v[82:83], v[224:225], s[18:19] op_sel_hi:[1,0]
	v_lshl_add_u64 v[246:247], v[160:161], 0, s[26:27]
	v_lshl_add_u64 v[246:247], v[246:247], 2, s[6:7]
	global_load_dwordx4 v[222:225], v[246:247], off
	global_load_dwordx4 v[226:229], v[246:247], off offset:16
	v_pk_fma_f32 v[76:77], v[76:77], v[132:133], v[80:81]
	v_pk_fma_f32 v[80:81], v[74:75], v[130:131], v[86:87]
	v_pk_fma_f32 v[74:75], v[72:73], v[128:129], v[84:85]
	v_pk_fma_f32 v[78:79], v[78:79], v[134:135], v[82:83]
	v_cvt_pk_bf16_f32 v72, v76, v77
	s_nop 0
	v_cvt_pk_bf16_f32 v73, v78, v79
	v_cvt_pk_bf16_f32 v74, v74, v75
	v_cvt_pk_bf16_f32 v75, v80, v81
	global_store_dwordx4 v[88:89], v[72:75], off
	s_nop 1
	v_lshl_add_u64 v[80:81], v[160:161], 0, s[20:21]
	s_waitcnt vmcnt(22)
	v_pk_mul_f32 v[72:73], v[230:231], s[18:19] op_sel_hi:[1,0]
	s_waitcnt vmcnt(21)
	v_pk_mul_f32 v[78:79], v[236:237], s[18:19] op_sel_hi:[1,0]
	v_pk_mul_f32 v[76:77], v[234:235], s[18:19] op_sel_hi:[1,0]
	v_pk_mul_f32 v[74:75], v[232:233], s[18:19] op_sel_hi:[1,0]
	v_lshl_add_u64 v[246:247], v[160:161], 0, s[26:27]
	v_lshl_add_u64 v[246:247], v[246:247], 2, s[6:7]
	global_load_dwordx4 v[230:233], v[246:247], off offset:512
	global_load_dwordx4 v[234:237], v[246:247], off offset:528
	v_pk_fma_f32 v[68:69], v[68:69], v[124:125], v[72:73]
	v_pk_fma_f32 v[72:73], v[66:67], v[122:123], v[78:79]
	v_pk_fma_f32 v[66:67], v[64:65], v[120:121], v[76:77]
	v_pk_fma_f32 v[70:71], v[70:71], v[126:127], v[74:75]
	v_cvt_pk_bf16_f32 v64, v68, v69
	s_nop 0
	v_cvt_pk_bf16_f32 v65, v70, v71
	v_cvt_pk_bf16_f32 v66, v66, v67
	v_cvt_pk_bf16_f32 v67, v72, v73
	global_store_dwordx4 v[88:89], v[64:67], off offset:256
	s_nop 1
	v_lshl_add_u64 v[72:73], v[80:81], 1, s[64:65]
	s_waitcnt vmcnt(23)
	v_pk_mul_f32 v[64:65], v[238:239], s[18:19] op_sel_hi:[1,0]
	s_waitcnt vmcnt(22)
	v_pk_mul_f32 v[70:71], v[244:245], s[18:19] op_sel_hi:[1,0]
	v_pk_mul_f32 v[68:69], v[242:243], s[18:19] op_sel_hi:[1,0]
	v_pk_mul_f32 v[66:67], v[240:241], s[18:19] op_sel_hi:[1,0]
	v_pk_fma_f32 v[60:61], v[60:61], v[132:133], v[64:65]
	v_pk_fma_f32 v[64:65], v[58:59], v[130:131], v[70:71]
	v_pk_fma_f32 v[58:59], v[56:57], v[128:129], v[68:69]
	v_pk_fma_f32 v[62:63], v[62:63], v[134:135], v[66:67]
	v_cvt_pk_bf16_f32 v56, v60, v61
	s_nop 0
	v_cvt_pk_bf16_f32 v57, v62, v63
	v_cvt_pk_bf16_f32 v58, v58, v59
	v_cvt_pk_bf16_f32 v59, v64, v65
	global_store_dwordx4 v[72:73], v[56:59], off
	s_nop 1
	v_lshl_add_u64 v[64:65], v[160:161], 0, s[22:23]
	s_waitcnt vmcnt(21)
	v_pk_mul_f32 v[56:57], v[182:183], s[18:19] op_sel_hi:[1,0]
	s_waitcnt vmcnt(20)
	v_pk_mul_f32 v[62:63], v[188:189], s[18:19] op_sel_hi:[1,0]
	v_pk_mul_f32 v[60:61], v[186:187], s[18:19] op_sel_hi:[1,0]
	v_pk_mul_f32 v[58:59], v[184:185], s[18:19] op_sel_hi:[1,0]
	v_pk_fma_f32 v[52:53], v[52:53], v[124:125], v[56:57]
	v_pk_fma_f32 v[56:57], v[50:51], v[122:123], v[62:63]
	v_pk_fma_f32 v[50:51], v[48:49], v[120:121], v[60:61]
	v_pk_fma_f32 v[54:55], v[54:55], v[126:127], v[58:59]
	v_cvt_pk_bf16_f32 v48, v52, v53
	s_nop 0
	v_cvt_pk_bf16_f32 v49, v54, v55
	v_cvt_pk_bf16_f32 v50, v50, v51
	v_cvt_pk_bf16_f32 v51, v56, v57
	global_store_dwordx4 v[72:73], v[48:51], off offset:256
	s_nop 1
	v_lshl_add_u64 v[56:57], v[64:65], 1, s[64:65]
	s_waitcnt vmcnt(19)
	v_pk_mul_f32 v[48:49], v[190:191], s[18:19] op_sel_hi:[1,0]
	s_waitcnt vmcnt(18)
	v_pk_mul_f32 v[54:55], v[196:197], s[18:19] op_sel_hi:[1,0]
	v_pk_mul_f32 v[52:53], v[194:195], s[18:19] op_sel_hi:[1,0]
	v_pk_mul_f32 v[50:51], v[192:193], s[18:19] op_sel_hi:[1,0]
	v_pk_fma_f32 v[44:45], v[44:45], v[132:133], v[48:49]
	v_pk_fma_f32 v[48:49], v[42:43], v[130:131], v[54:55]
	v_pk_fma_f32 v[42:43], v[40:41], v[128:129], v[52:53]
	v_pk_fma_f32 v[46:47], v[46:47], v[134:135], v[50:51]
	v_cvt_pk_bf16_f32 v40, v44, v45
	s_nop 0
	v_cvt_pk_bf16_f32 v41, v46, v47
	v_cvt_pk_bf16_f32 v42, v42, v43
	v_cvt_pk_bf16_f32 v43, v48, v49
	global_store_dwordx4 v[56:57], v[40:43], off
	s_nop 1
	v_lshl_add_u64 v[48:49], v[160:161], 0, s[24:25]
	s_waitcnt vmcnt(17)
	v_pk_mul_f32 v[40:41], v[198:199], s[18:19] op_sel_hi:[1,0]
	s_waitcnt vmcnt(16)
	v_pk_mul_f32 v[46:47], v[204:205], s[18:19] op_sel_hi:[1,0]
	v_pk_mul_f32 v[44:45], v[202:203], s[18:19] op_sel_hi:[1,0]
	v_pk_mul_f32 v[42:43], v[200:201], s[18:19] op_sel_hi:[1,0]
	v_pk_fma_f32 v[36:37], v[36:37], v[124:125], v[40:41]
	v_pk_fma_f32 v[40:41], v[34:35], v[122:123], v[46:47]
	v_pk_fma_f32 v[34:35], v[32:33], v[120:121], v[44:45]
	v_pk_fma_f32 v[38:39], v[38:39], v[126:127], v[42:43]
	v_cvt_pk_bf16_f32 v32, v36, v37
	s_nop 0
	v_cvt_pk_bf16_f32 v33, v38, v39
	v_cvt_pk_bf16_f32 v34, v34, v35
	v_cvt_pk_bf16_f32 v35, v40, v41
	global_store_dwordx4 v[56:57], v[32:35], off offset:256
	s_nop 1
	v_lshl_add_u64 v[40:41], v[48:49], 1, s[64:65]
	s_waitcnt vmcnt(15)
	v_pk_mul_f32 v[32:33], v[206:207], s[18:19] op_sel_hi:[1,0]
	s_waitcnt vmcnt(14)
	v_pk_mul_f32 v[38:39], v[212:213], s[18:19] op_sel_hi:[1,0]
	v_pk_mul_f32 v[36:37], v[210:211], s[18:19] op_sel_hi:[1,0]
	v_pk_mul_f32 v[34:35], v[208:209], s[18:19] op_sel_hi:[1,0]
	v_pk_fma_f32 v[28:29], v[28:29], v[132:133], v[32:33]
	v_pk_fma_f32 v[32:33], v[26:27], v[130:131], v[38:39]
	v_pk_fma_f32 v[26:27], v[24:25], v[128:129], v[36:37]
	v_pk_fma_f32 v[30:31], v[30:31], v[134:135], v[34:35]
	v_cvt_pk_bf16_f32 v24, v28, v29
	s_nop 0
	v_cvt_pk_bf16_f32 v25, v30, v31
	v_cvt_pk_bf16_f32 v26, v26, v27
	v_cvt_pk_bf16_f32 v27, v32, v33
	global_store_dwordx4 v[40:41], v[24:27], off
	s_nop 1
	v_lshl_add_u64 v[32:33], v[160:161], 0, s[26:27]
	s_waitcnt vmcnt(13)
	v_pk_mul_f32 v[24:25], v[214:215], s[18:19] op_sel_hi:[1,0]
	s_waitcnt vmcnt(12)
	v_pk_mul_f32 v[30:31], v[220:221], s[18:19] op_sel_hi:[1,0]
	v_pk_mul_f32 v[28:29], v[218:219], s[18:19] op_sel_hi:[1,0]
	v_pk_mul_f32 v[26:27], v[216:217], s[18:19] op_sel_hi:[1,0]
	v_pk_fma_f32 v[20:21], v[20:21], v[124:125], v[24:25]
	v_pk_fma_f32 v[24:25], v[18:19], v[122:123], v[30:31]
	v_pk_fma_f32 v[18:19], v[16:17], v[120:121], v[28:29]
	v_pk_fma_f32 v[22:23], v[22:23], v[126:127], v[26:27]
	v_cvt_pk_bf16_f32 v16, v20, v21
	s_nop 0
	v_cvt_pk_bf16_f32 v17, v22, v23
	v_cvt_pk_bf16_f32 v18, v18, v19
	v_cvt_pk_bf16_f32 v19, v24, v25
	global_store_dwordx4 v[40:41], v[16:19], off offset:256
	s_nop 1
	v_lshl_add_u64 v[24:25], v[32:33], 1, s[64:65]
	s_waitcnt vmcnt(11)
	v_pk_mul_f32 v[16:17], v[222:223], s[18:19] op_sel_hi:[1,0]
	s_waitcnt vmcnt(10)
	v_pk_mul_f32 v[22:23], v[228:229], s[18:19] op_sel_hi:[1,0]
	v_pk_mul_f32 v[20:21], v[226:227], s[18:19] op_sel_hi:[1,0]
	v_pk_mul_f32 v[18:19], v[224:225], s[18:19] op_sel_hi:[1,0]
	v_pk_fma_f32 v[12:13], v[12:13], v[132:133], v[16:17]
	v_pk_fma_f32 v[16:17], v[10:11], v[130:131], v[22:23]
	v_pk_fma_f32 v[10:11], v[8:9], v[128:129], v[20:21]
	v_pk_fma_f32 v[14:15], v[14:15], v[134:135], v[18:19]
	v_cvt_pk_bf16_f32 v8, v12, v13
	s_nop 0
	v_cvt_pk_bf16_f32 v9, v14, v15
	v_cvt_pk_bf16_f32 v10, v10, v11
	v_cvt_pk_bf16_f32 v11, v16, v17
	global_store_dwordx4 v[24:25], v[8:11], off
	s_nop 1
	s_waitcnt vmcnt(9)
	v_pk_mul_f32 v[8:9], v[230:231], s[18:19] op_sel_hi:[1,0]
	s_waitcnt vmcnt(8)
	v_pk_mul_f32 v[14:15], v[236:237], s[18:19] op_sel_hi:[1,0]
	v_pk_mul_f32 v[12:13], v[234:235], s[18:19] op_sel_hi:[1,0]
	v_pk_mul_f32 v[10:11], v[232:233], s[18:19] op_sel_hi:[1,0]
	v_pk_fma_f32 v[4:5], v[4:5], v[124:125], v[8:9]
	v_pk_fma_f32 v[8:9], v[2:3], v[122:123], v[14:15]
	v_pk_fma_f32 v[2:3], v[0:1], v[120:121], v[12:13]
	v_pk_fma_f32 v[6:7], v[6:7], v[126:127], v[10:11]
	v_cvt_pk_bf16_f32 v0, v4, v5
	s_nop 0
	v_cvt_pk_bf16_f32 v1, v6, v7
	v_cvt_pk_bf16_f32 v2, v2, v3
	v_cvt_pk_bf16_f32 v3, v8, v9
	global_store_dwordx4 v[24:25], v[0:3], off offset:256
	s_nop 1
	s_cbranch_vccnz .LBB0_333
	s_andn2_b64 vcc, exec, s[10:11]
	s_cbranch_vccnz .LBB0_332
	s_barrier
	s_branch .LBB0_332
